# v3 + 4 instead of 2 late w_down transposition units per expert moved from MIX to the idle last round of MOE1
# baseline (speedup 1.0000x reference)
.LBB0_882:
	s_or_b64 exec, exec, s[8:9]
	s_waitcnt lgkmcnt(0)
	s_barrier
	ds_read_b32 v2, v237
	s_waitcnt lgkmcnt(0)
	v_readfirstlane_b32 s2, v2
	s_cmpk_gt_i32 s2, 0x47f
	s_cselect_b64 s[8:9], -1, 0
	s_and_b64 vcc, exec, s[8:9]
	s_cbranch_vccnz .LBB0_888
	s_mul_hi_i32 s3, s2, 0x71c71c72
	s_lshr_b32 s10, s3, 31
	s_ashr_i32 s3, s3, 4
	s_add_i32 s12, s3, s10
	s_mul_i32 s3, s12, 36
	s_sub_i32 s2, s2, s3
	s_mov_b64 s[14:15], s[44:45]
	v_mov_b32_e32 v4, v0
	s_add_i32 s3, s2, 4
	s_load_dwordx2 s[10:11], s[14:15], 0xd8
	s_cmp_lt_i32 s2, 32
	s_cselect_b32 s3, s2, s3
	v_readfirstlane_b32 s2, v4
	s_ashr_i32 s2, s2, 6
	v_lshlrev_b32_e32 v2, 1, v4
	v_lshlrev_b32_e32 v4, 2, v4
	s_cmp_gt_i32 s3, 31
	v_and_b32_e32 v2, 0x70, v2
	v_and_b32_e32 v134, 28, v4
	s_mov_b64 s[16:17], -1
	s_cbranch_scc0 .LBB0_885
	s_lshl_b32 s13, s3, 6
	s_add_i32 s13, s13, 0x7ffff800
	s_load_dwordx2 s[16:17], s[14:15], 0xc8
	s_and_b32 s79, s13, 0x7fffff80
	s_lshl_b32 s13, s3, 10
	s_and_b32 s13, s13, 0x400
	s_lshl_b32 s18, s2, 7
	s_add_i32 s18, s18, s13
	s_ashr_i32 s13, s12, 31
	s_lshl_b64 s[24:25], s[12:13], 23
	v_lshlrev_b32_e32 v135, 11, v2
	s_waitcnt lgkmcnt(0)
	s_add_u32 s24, s16, s24
	v_add_u32_e32 v4, s18, v135
	s_addc_u32 s19, s17, s25
	s_lshl_b64 s[16:17], s[12:13], 21
	v_or_b32_e32 v4, v4, v134
	s_lshl_b32 s13, s79, 13
	s_and_b32 s25, s19, 0xffff
	v_lshlrev_b32_e32 v4, 2, v4
	s_or_b32 s19, s13, 0x2000
	buffer_load_dwordx4 v[68:71], v4, s[24:27], s13 offen nt
	buffer_load_dwordx4 v[88:91], v4, s[24:27], s19 offen nt
	s_or_b32 s40, s13, 0x8000
	s_or_b32 s41, s13, 0xa000
	buffer_load_dwordx4 v[104:107], v4, s[24:27], s40 offen nt
	buffer_load_dwordx4 v[116:119], v4, s[24:27], s41 offen nt
	s_or_b32 s46, s13, 0x10000
	s_or_b32 s47, s13, 0x12000
	buffer_load_dwordx4 v[72:75], v4, s[24:27], s46 offen nt
	buffer_load_dwordx4 v[80:83], v4, s[24:27], s47 offen nt
	s_or_b32 s74, s13, 0x18000
	s_or_b32 s75, s13, 0x1a000
	buffer_load_dwordx4 v[76:79], v4, s[24:27], s74 offen nt
	buffer_load_dwordx4 v[96:99], v4, s[24:27], s75 offen nt
	s_or_b32 s22, s13, 0x4000
	s_or_b32 s33, s13, 0x6000
	s_or_b32 s50, s13, 0x14000
	s_or_b32 s51, s13, 0x16000
	buffer_load_dwordx4 v[100:103], v4, s[24:27], s22 offen nt
	buffer_load_dwordx4 v[112:115], v4, s[24:27], s33 offen nt
	s_or_b32 s42, s13, 0xc000
	s_or_b32 s43, s13, 0xe000
	buffer_load_dwordx4 v[84:87], v4, s[24:27], s50 offen nt
	buffer_load_dwordx4 v[92:95], v4, s[24:27], s51 offen nt
	s_or_b32 s76, s13, 0x1c000
	s_or_b32 s77, s13, 0x1e000
	buffer_load_dwordx4 v[124:127], v4, s[24:27], s42 offen nt
	buffer_load_dwordx4 v[128:131], v4, s[24:27], s43 offen nt
	buffer_load_dwordx4 v[108:111], v4, s[24:27], s76 offen nt
	buffer_load_dwordx4 v[120:123], v4, s[24:27], s77 offen nt
	s_or_b32 s78, s18, 32
	v_add_u32_e32 v4, s78, v135
	v_or_b32_e32 v4, v4, v134
	v_lshlrev_b32_e32 v16, 2, v4
	buffer_load_dwordx4 v[52:55], v16, s[24:27], s13 offen nt
	buffer_load_dwordx4 v[56:59], v16, s[24:27], s19 offen nt
	buffer_load_dwordx4 v[60:63], v16, s[24:27], s22 offen nt
	buffer_load_dwordx4 v[64:67], v16, s[24:27], s33 offen nt
	buffer_load_dwordx4 v[36:39], v16, s[24:27], s40 offen nt
	buffer_load_dwordx4 v[40:43], v16, s[24:27], s41 offen nt
	buffer_load_dwordx4 v[44:47], v16, s[24:27], s42 offen nt
	buffer_load_dwordx4 v[48:51], v16, s[24:27], s43 offen nt
	buffer_load_dwordx4 v[20:23], v16, s[24:27], s46 offen nt
	buffer_load_dwordx4 v[24:27], v16, s[24:27], s47 offen nt
	buffer_load_dwordx4 v[28:31], v16, s[24:27], s50 offen nt
	buffer_load_dwordx4 v[32:35], v16, s[24:27], s51 offen nt
	buffer_load_dwordx4 v[4:7], v16, s[24:27], s74 offen nt
	buffer_load_dwordx4 v[8:11], v16, s[24:27], s75 offen nt
	buffer_load_dwordx4 v[12:15], v16, s[24:27], s76 offen nt
	s_nop 0
	buffer_load_dwordx4 v[16:19], v16, s[24:27], s77 offen nt
	v_mov_b32_e32 v138, v3
	v_mov_b32_e32 v139, v3
	v_mov_b32_e32 v140, v3
	v_mov_b32_e32 v141, v3
	s_add_u32 s16, s10, s16
	s_addc_u32 s17, s11, s17
	s_add_u32 s16, s16, s79
	v_or_b32_e32 v132, s18, v134
	s_addc_u32 s17, s17, 0
	v_lshl_add_u64 v[136:137], s[16:17], 0, v[2:3]
	s_mov_b64 s[16:17], 0x14c00000
	v_ashrrev_i32_e32 v133, 31, v132
	v_lshl_add_u64 v[136:137], v[136:137], 0, s[16:17]
	v_lshlrev_b64 v[142:143], 10, v[132:133]
	v_lshl_add_u64 v[142:143], v[136:137], 0, v[142:143]
	s_or_b32 s16, s18, 64
	s_or_b32 s17, s18, 0x60
	s_waitcnt vmcnt(31)
	v_mul_f32_e32 v68, 0x42800000, v68
	s_waitcnt vmcnt(30)
	v_mul_f32_e32 v88, 0x42800000, v88
	v_cvt_pk_fp8_f32 v138, v68, v88
	s_waitcnt vmcnt(29)
	v_mul_f32_e32 v68, 0x42800000, v104
	s_waitcnt vmcnt(28)
	v_mul_f32_e32 v88, 0x42800000, v116
	v_cvt_pk_fp8_f32 v139, v68, v88
	s_waitcnt vmcnt(27)
	v_mul_f32_e32 v68, 0x42800000, v72
	s_waitcnt vmcnt(26)
	v_mul_f32_e32 v72, 0x42800000, v80
	v_cvt_pk_fp8_f32 v140, v68, v72
	s_waitcnt vmcnt(25)
	v_mul_f32_e32 v68, 0x42800000, v76
	s_waitcnt vmcnt(24)
	v_mul_f32_e32 v72, 0x42800000, v96
	v_cvt_pk_fp8_f32 v141, v68, v72
	v_mul_f32_e32 v68, 0x42800000, v69
	v_mul_f32_e32 v69, 0x42800000, v89
	s_waitcnt vmcnt(23)
	v_mul_f32_e32 v100, 0x42800000, v100
	s_waitcnt vmcnt(22)
	v_mul_f32_e32 v112, 0x42800000, v112
	v_cvt_pk_fp8_f32 v138, v100, v112 op_sel:[0,0,1]
	v_mul_f32_e32 v72, 0x42800000, v101
	s_waitcnt vmcnt(21)
	v_mul_f32_e32 v80, 0x42800000, v84
	s_waitcnt vmcnt(20)
	v_mul_f32_e32 v84, 0x42800000, v92
	v_cvt_pk_fp8_f32 v140, v80, v84 op_sel:[0,0,1]
	s_waitcnt vmcnt(15)
	v_mul_f32_e32 v52, 0x42800000, v52
	v_mul_f32_e32 v100, 0x42800000, v124
	v_mul_f32_e32 v104, 0x42800000, v128
	v_mul_f32_e32 v76, 0x42800000, v108
	v_mul_f32_e32 v80, 0x42800000, v120
	v_cvt_pk_fp8_f32 v139, v100, v104 op_sel:[0,0,1]
	v_cvt_pk_fp8_f32 v141, v76, v80 op_sel:[0,0,1]
	v_mul_f32_e32 v76, 0x42800000, v113
	s_waitcnt vmcnt(14)
	v_mul_f32_e32 v56, 0x42800000, v56
	s_waitcnt vmcnt(11)
	v_mul_f32_e32 v36, 0x42800000, v36
	global_store_dwordx4 v[142:143], v[138:141], off nt
	s_waitcnt vmcnt(11)
	v_mul_f32_e32 v40, 0x42800000, v40
	s_waitcnt vmcnt(8)
	v_mul_f32_e32 v20, 0x42800000, v20
	v_mov_b32_e32 v138, v3
	v_cvt_pk_fp8_f32 v138, v68, v69
	v_mul_f32_e32 v68, 0x42800000, v105
	v_mul_f32_e32 v69, 0x42800000, v117
	v_mov_b32_e32 v139, v3
	v_cvt_pk_fp8_f32 v139, v68, v69
	v_mul_f32_e32 v68, 0x42800000, v73
	v_mul_f32_e32 v69, 0x42800000, v81
	v_mov_b32_e32 v140, v3
	v_cvt_pk_fp8_f32 v140, v68, v69
	v_mul_f32_e32 v68, 0x42800000, v77
	v_mul_f32_e32 v69, 0x42800000, v97
	v_mov_b32_e32 v141, v3
	v_cvt_pk_fp8_f32 v141, v68, v69
	v_cvt_pk_fp8_f32 v138, v72, v76 op_sel:[0,0,1]
	v_mul_f32_e32 v72, 0x42800000, v125
	v_mul_f32_e32 v76, 0x42800000, v129
	v_cvt_pk_fp8_f32 v139, v72, v76 op_sel:[0,0,1]
	v_mul_f32_e32 v72, 0x42800000, v85
	v_mul_f32_e32 v73, 0x42800000, v93
	v_cvt_pk_fp8_f32 v140, v72, v73 op_sel:[0,0,1]
	v_mul_f32_e32 v72, 0x42800000, v109
	v_mul_f32_e32 v73, 0x42800000, v121
	v_cvt_pk_fp8_f32 v141, v72, v73 op_sel:[0,0,1]
	v_or_b32_e32 v68, 1, v132
	v_ashrrev_i32_e32 v69, 31, v68
	v_lshlrev_b64 v[68:69], 10, v[68:69]
	v_lshl_add_u64 v[68:69], v[136:137], 0, v[68:69]
	global_store_dwordx4 v[68:69], v[138:141], off nt
	v_mul_f32_e32 v68, 0x42800000, v70
	v_mul_f32_e32 v69, 0x42800000, v90
	v_mov_b32_e32 v138, v3
	v_cvt_pk_fp8_f32 v138, v68, v69
	v_mul_f32_e32 v68, 0x42800000, v106
	v_mul_f32_e32 v69, 0x42800000, v118
	v_mov_b32_e32 v139, v3
	v_cvt_pk_fp8_f32 v139, v68, v69
	v_mul_f32_e32 v68, 0x42800000, v74
	v_mul_f32_e32 v69, 0x42800000, v82
	v_mov_b32_e32 v140, v3
	v_cvt_pk_fp8_f32 v140, v68, v69
	v_mul_f32_e32 v68, 0x42800000, v78
	v_mul_f32_e32 v69, 0x42800000, v98
	v_mov_b32_e32 v141, v3
	v_mul_f32_e32 v70, 0x42800000, v102
	v_mul_f32_e32 v72, 0x42800000, v114
	v_cvt_pk_fp8_f32 v141, v68, v69
	v_cvt_pk_fp8_f32 v138, v70, v72 op_sel:[0,0,1]
	v_mul_f32_e32 v70, 0x42800000, v126
	v_mul_f32_e32 v72, 0x42800000, v130
	v_cvt_pk_fp8_f32 v139, v70, v72 op_sel:[0,0,1]
	v_mul_f32_e32 v70, 0x42800000, v86
	v_mul_f32_e32 v72, 0x42800000, v94
	v_cvt_pk_fp8_f32 v140, v70, v72 op_sel:[0,0,1]
	v_mul_f32_e32 v70, 0x42800000, v110
	v_mul_f32_e32 v72, 0x42800000, v122
	v_cvt_pk_fp8_f32 v141, v70, v72 op_sel:[0,0,1]
	v_or_b32_e32 v68, 2, v132
	v_ashrrev_i32_e32 v69, 31, v68
	v_lshlrev_b64 v[68:69], 10, v[68:69]
	v_lshl_add_u64 v[68:69], v[136:137], 0, v[68:69]
	global_store_dwordx4 v[68:69], v[138:141], off nt
	v_mul_f32_e32 v69, 0x42800000, v71
	v_mul_f32_e32 v70, 0x42800000, v91
	v_mov_b32_e32 v68, v3
	v_cvt_pk_fp8_f32 v68, v69, v70
	v_mul_f32_e32 v71, 0x42800000, v103
	v_mul_f32_e32 v72, 0x42800000, v115
	v_mul_f32_e32 v70, 0x42800000, v107
	v_cvt_pk_fp8_f32 v68, v71, v72 op_sel:[0,0,1]
	v_mul_f32_e32 v71, 0x42800000, v119
	v_mov_b32_e32 v69, v3
	v_cvt_pk_fp8_f32 v69, v70, v71
	v_mul_f32_e32 v72, 0x42800000, v127
	v_mul_f32_e32 v73, 0x42800000, v131
	v_mul_f32_e32 v71, 0x42800000, v75
	v_cvt_pk_fp8_f32 v69, v72, v73 op_sel:[0,0,1]
	v_mul_f32_e32 v72, 0x42800000, v83
	v_mov_b32_e32 v70, v3
	v_cvt_pk_fp8_f32 v70, v71, v72
	v_mul_f32_e32 v73, 0x42800000, v87
	v_mul_f32_e32 v74, 0x42800000, v95
	v_mul_f32_e32 v72, 0x42800000, v79
	v_cvt_pk_fp8_f32 v70, v73, v74 op_sel:[0,0,1]
	v_mul_f32_e32 v73, 0x42800000, v99
	v_mov_b32_e32 v71, v3
	v_cvt_pk_fp8_f32 v71, v72, v73
	v_mul_f32_e32 v74, 0x42800000, v111
	v_mul_f32_e32 v75, 0x42800000, v123
	v_or_b32_e32 v72, 3, v132
	v_cvt_pk_fp8_f32 v71, v74, v75 op_sel:[0,0,1]
	v_ashrrev_i32_e32 v73, 31, v72
	v_lshlrev_b64 v[72:73], 10, v[72:73]
	v_lshl_add_u64 v[72:73], v[136:137], 0, v[72:73]
	global_store_dwordx4 v[72:73], v[68:71], off nt
	v_mov_b32_e32 v138, v3
	v_mov_b32_e32 v139, v3
	v_add_u32_e32 v68, s16, v135
	s_waitcnt vmcnt(10)
	v_mul_f32_e32 v24, 0x42800000, v24
	v_mov_b32_e32 v140, v3
	s_waitcnt vmcnt(7)
	v_mul_f32_e32 v4, 0x42800000, v4
	s_waitcnt vmcnt(6)
	v_mul_f32_e32 v8, 0x42800000, v8
	v_mov_b32_e32 v141, v3
	v_or_b32_e32 v68, v68, v134
	v_cvt_pk_fp8_f32 v138, v52, v56
	v_cvt_pk_fp8_f32 v139, v36, v40
	v_cvt_pk_fp8_f32 v140, v20, v24
	v_cvt_pk_fp8_f32 v141, v4, v8
	v_lshlrev_b32_e32 v80, 2, v68
	buffer_load_dwordx4 v[116:119], v80, s[24:27], s13 offen nt
	buffer_load_dwordx4 v[120:123], v80, s[24:27], s19 offen nt
	buffer_load_dwordx4 v[124:127], v80, s[24:27], s22 offen nt
	buffer_load_dwordx4 v[128:131], v80, s[24:27], s33 offen nt
	buffer_load_dwordx4 v[100:103], v80, s[24:27], s40 offen nt
	buffer_load_dwordx4 v[104:107], v80, s[24:27], s41 offen nt
	buffer_load_dwordx4 v[108:111], v80, s[24:27], s42 offen nt
	buffer_load_dwordx4 v[112:115], v80, s[24:27], s43 offen nt
	buffer_load_dwordx4 v[84:87], v80, s[24:27], s46 offen nt
	buffer_load_dwordx4 v[88:91], v80, s[24:27], s47 offen nt
	buffer_load_dwordx4 v[92:95], v80, s[24:27], s50 offen nt
	buffer_load_dwordx4 v[96:99], v80, s[24:27], s51 offen nt
	buffer_load_dwordx4 v[68:71], v80, s[24:27], s74 offen nt
	buffer_load_dwordx4 v[72:75], v80, s[24:27], s75 offen nt
	buffer_load_dwordx4 v[76:79], v80, s[24:27], s76 offen nt
	s_nop 0
	buffer_load_dwordx4 v[80:83], v80, s[24:27], s77 offen nt
	v_mul_f32_e32 v60, 0x42800000, v60
	v_mul_f32_e32 v64, 0x42800000, v64
	v_mul_f32_e32 v44, 0x42800000, v44
	v_mul_f32_e32 v48, 0x42800000, v48
	v_mul_f32_e32 v28, 0x42800000, v28
	v_mul_f32_e32 v32, 0x42800000, v32
	s_waitcnt vmcnt(21)
	v_mul_f32_e32 v12, 0x42800000, v12
	s_waitcnt vmcnt(20)
	v_mul_f32_e32 v16, 0x42800000, v16
	v_or_b32_e32 v132, s78, v134
	v_cvt_pk_fp8_f32 v138, v60, v64 op_sel:[0,0,1]
	v_cvt_pk_fp8_f32 v139, v44, v48 op_sel:[0,0,1]
	v_cvt_pk_fp8_f32 v140, v28, v32 op_sel:[0,0,1]
	v_cvt_pk_fp8_f32 v141, v12, v16 op_sel:[0,0,1]
	v_ashrrev_i32_e32 v133, 31, v132
	v_lshlrev_b64 v[142:143], 10, v[132:133]
	v_lshl_add_u64 v[142:143], v[136:137], 0, v[142:143]
	global_store_dwordx4 v[142:143], v[138:141], off nt
	v_mul_f32_e32 v4, 0x42800000, v53
	v_mul_f32_e32 v8, 0x42800000, v57
	v_mov_b32_e32 v138, v3
	v_cvt_pk_fp8_f32 v138, v4, v8
	v_mul_f32_e32 v4, 0x42800000, v37
	v_mul_f32_e32 v8, 0x42800000, v41
	v_mov_b32_e32 v139, v3
	v_cvt_pk_fp8_f32 v139, v4, v8
	v_mul_f32_e32 v4, 0x42800000, v21
	v_mul_f32_e32 v8, 0x42800000, v25
	v_mov_b32_e32 v140, v3
	v_cvt_pk_fp8_f32 v140, v4, v8
	v_mul_f32_e32 v4, 0x42800000, v5
	v_mul_f32_e32 v5, 0x42800000, v9
	v_mov_b32_e32 v141, v3
	v_cvt_pk_fp8_f32 v141, v4, v5
	v_mul_f32_e32 v12, 0x42800000, v61
	v_mul_f32_e32 v16, 0x42800000, v65
	v_cvt_pk_fp8_f32 v138, v12, v16 op_sel:[0,0,1]
	v_mul_f32_e32 v12, 0x42800000, v45
	v_mul_f32_e32 v16, 0x42800000, v49
	v_cvt_pk_fp8_f32 v139, v12, v16 op_sel:[0,0,1]
	v_mul_f32_e32 v12, 0x42800000, v29
	v_mul_f32_e32 v16, 0x42800000, v33
	v_mul_f32_e32 v8, 0x42800000, v13
	v_mul_f32_e32 v9, 0x42800000, v17
	v_cvt_pk_fp8_f32 v140, v12, v16 op_sel:[0,0,1]
	v_cvt_pk_fp8_f32 v141, v8, v9 op_sel:[0,0,1]
	v_or_b32_e32 v4, 1, v132
	v_ashrrev_i32_e32 v5, 31, v4
	v_lshlrev_b64 v[4:5], 10, v[4:5]
	v_lshl_add_u64 v[4:5], v[136:137], 0, v[4:5]
	global_store_dwordx4 v[4:5], v[138:141], off nt
	v_mul_f32_e32 v4, 0x42800000, v54
	v_mul_f32_e32 v5, 0x42800000, v58
	v_mov_b32_e32 v138, v3
	v_cvt_pk_fp8_f32 v138, v4, v5
	v_mul_f32_e32 v4, 0x42800000, v38
	v_mul_f32_e32 v5, 0x42800000, v42
	v_mov_b32_e32 v139, v3
	v_cvt_pk_fp8_f32 v139, v4, v5
	v_mul_f32_e32 v4, 0x42800000, v22
	v_mul_f32_e32 v5, 0x42800000, v26
	v_mov_b32_e32 v140, v3
	v_cvt_pk_fp8_f32 v140, v4, v5
	v_mul_f32_e32 v4, 0x42800000, v6
	v_mul_f32_e32 v5, 0x42800000, v10
	v_mov_b32_e32 v141, v3
	v_mul_f32_e32 v8, 0x42800000, v62
	v_mul_f32_e32 v9, 0x42800000, v66
	v_cvt_pk_fp8_f32 v141, v4, v5
	v_cvt_pk_fp8_f32 v138, v8, v9 op_sel:[0,0,1]
	v_mul_f32_e32 v8, 0x42800000, v46
	v_mul_f32_e32 v9, 0x42800000, v50
	v_cvt_pk_fp8_f32 v139, v8, v9 op_sel:[0,0,1]
	v_mul_f32_e32 v8, 0x42800000, v30
	v_mul_f32_e32 v9, 0x42800000, v34
	v_cvt_pk_fp8_f32 v140, v8, v9 op_sel:[0,0,1]
	v_mul_f32_e32 v6, 0x42800000, v14
	v_mul_f32_e32 v8, 0x42800000, v18
	v_cvt_pk_fp8_f32 v141, v6, v8 op_sel:[0,0,1]
	v_or_b32_e32 v4, 2, v132
	v_ashrrev_i32_e32 v5, 31, v4
	v_lshlrev_b64 v[4:5], 10, v[4:5]
	v_lshl_add_u64 v[4:5], v[136:137], 0, v[4:5]
	global_store_dwordx4 v[4:5], v[138:141], off nt
	v_mul_f32_e32 v5, 0x42800000, v55
	v_mul_f32_e32 v6, 0x42800000, v59
	v_mov_b32_e32 v4, v3
	v_cvt_pk_fp8_f32 v4, v5, v6
	v_mul_f32_e32 v8, 0x42800000, v63
	v_mul_f32_e32 v9, 0x42800000, v67
	v_mul_f32_e32 v6, 0x42800000, v39
	v_cvt_pk_fp8_f32 v4, v8, v9 op_sel:[0,0,1]
	v_mul_f32_e32 v8, 0x42800000, v43
	v_mov_b32_e32 v5, v3
	v_cvt_pk_fp8_f32 v5, v6, v8
	v_mul_f32_e32 v9, 0x42800000, v47
	v_mul_f32_e32 v10, 0x42800000, v51
	v_mul_f32_e32 v8, 0x42800000, v23
	v_cvt_pk_fp8_f32 v5, v9, v10 op_sel:[0,0,1]
	v_mul_f32_e32 v9, 0x42800000, v27
	v_mov_b32_e32 v6, v3
	v_cvt_pk_fp8_f32 v6, v8, v9
	v_mul_f32_e32 v8, 0x42800000, v7
	v_mul_f32_e32 v9, 0x42800000, v11
	v_mov_b32_e32 v7, v3
	v_cvt_pk_fp8_f32 v7, v8, v9
	v_mul_f32_e32 v10, 0x42800000, v31
	v_mul_f32_e32 v12, 0x42800000, v35
	v_cvt_pk_fp8_f32 v6, v10, v12 op_sel:[0,0,1]
	v_mul_f32_e32 v10, 0x42800000, v15
	v_mul_f32_e32 v11, 0x42800000, v19
	v_cvt_pk_fp8_f32 v7, v10, v11 op_sel:[0,0,1]
	v_or_b32_e32 v8, 3, v132
	v_ashrrev_i32_e32 v9, 31, v8
	v_lshlrev_b64 v[8:9], 10, v[8:9]
	v_lshl_add_u64 v[8:9], v[136:137], 0, v[8:9]
	global_store_dwordx4 v[8:9], v[4:7], off nt
	s_waitcnt vmcnt(19)
	v_mul_f32_e32 v116, 0x42800000, v116
	s_waitcnt vmcnt(18)
	v_mul_f32_e32 v120, 0x42800000, v120
	v_add_u32_e32 v4, s17, v135
	v_or_b32_e32 v4, v4, v134
	v_lshlrev_b32_e32 v16, 2, v4
	buffer_load_dwordx4 v[52:55], v16, s[24:27], s13 offen nt
	buffer_load_dwordx4 v[56:59], v16, s[24:27], s19 offen nt
	buffer_load_dwordx4 v[60:63], v16, s[24:27], s22 offen nt
	buffer_load_dwordx4 v[64:67], v16, s[24:27], s33 offen nt
	buffer_load_dwordx4 v[36:39], v16, s[24:27], s40 offen nt
	buffer_load_dwordx4 v[40:43], v16, s[24:27], s41 offen nt
	buffer_load_dwordx4 v[44:47], v16, s[24:27], s42 offen nt
	buffer_load_dwordx4 v[48:51], v16, s[24:27], s43 offen nt
	buffer_load_dwordx4 v[20:23], v16, s[24:27], s46 offen nt
	buffer_load_dwordx4 v[24:27], v16, s[24:27], s47 offen nt
	buffer_load_dwordx4 v[28:31], v16, s[24:27], s50 offen nt
	buffer_load_dwordx4 v[32:35], v16, s[24:27], s51 offen nt
	buffer_load_dwordx4 v[4:7], v16, s[24:27], s74 offen nt
	buffer_load_dwordx4 v[8:11], v16, s[24:27], s75 offen nt
	buffer_load_dwordx4 v[12:15], v16, s[24:27], s76 offen nt
	s_nop 0
	buffer_load_dwordx4 v[16:19], v16, s[24:27], s77 offen nt
	v_mov_b32_e32 v138, v3
	s_waitcnt vmcnt(31)
	v_mul_f32_e32 v100, 0x42800000, v100
	s_waitcnt vmcnt(30)
	v_mul_f32_e32 v104, 0x42800000, v104
	v_mov_b32_e32 v139, v3
	s_waitcnt vmcnt(27)
	v_mul_f32_e32 v84, 0x42800000, v84
	s_waitcnt vmcnt(26)
	v_mul_f32_e32 v88, 0x42800000, v88
	v_mov_b32_e32 v140, v3
	s_waitcnt vmcnt(23)
	v_mul_f32_e32 v68, 0x42800000, v68
	s_waitcnt vmcnt(22)
	v_mul_f32_e32 v72, 0x42800000, v72
	v_mov_b32_e32 v141, v3
	v_cvt_pk_fp8_f32 v138, v116, v120
	v_cvt_pk_fp8_f32 v139, v100, v104
	v_cvt_pk_fp8_f32 v140, v84, v88
	v_cvt_pk_fp8_f32 v141, v68, v72
	v_mul_f32_e32 v124, 0x42800000, v124
	v_mul_f32_e32 v128, 0x42800000, v128
	v_mul_f32_e32 v108, 0x42800000, v108
	v_mul_f32_e32 v112, 0x42800000, v112
	v_mul_f32_e32 v92, 0x42800000, v92
	v_mul_f32_e32 v96, 0x42800000, v96
	s_waitcnt vmcnt(21)
	v_mul_f32_e32 v76, 0x42800000, v76
	s_waitcnt vmcnt(20)
	v_mul_f32_e32 v80, 0x42800000, v80
	v_or_b32_e32 v132, s16, v134
	v_cvt_pk_fp8_f32 v138, v124, v128 op_sel:[0,0,1]
	v_cvt_pk_fp8_f32 v139, v108, v112 op_sel:[0,0,1]
	v_cvt_pk_fp8_f32 v140, v92, v96 op_sel:[0,0,1]
	v_cvt_pk_fp8_f32 v141, v76, v80 op_sel:[0,0,1]
	v_ashrrev_i32_e32 v133, 31, v132
	v_lshlrev_b64 v[142:143], 10, v[132:133]
	v_lshl_add_u64 v[142:143], v[136:137], 0, v[142:143]
	global_store_dwordx4 v[142:143], v[138:141], off nt
	v_mul_f32_e32 v68, 0x42800000, v117
	v_mul_f32_e32 v72, 0x42800000, v121
	v_mov_b32_e32 v138, v3
	v_cvt_pk_fp8_f32 v138, v68, v72
	v_mul_f32_e32 v68, 0x42800000, v101
	v_mul_f32_e32 v72, 0x42800000, v105
	v_mov_b32_e32 v139, v3
	v_cvt_pk_fp8_f32 v139, v68, v72
	v_mul_f32_e32 v68, 0x42800000, v85
	v_mul_f32_e32 v72, 0x42800000, v89
	v_mov_b32_e32 v140, v3
	v_cvt_pk_fp8_f32 v140, v68, v72
	v_mul_f32_e32 v68, 0x42800000, v69
	v_mul_f32_e32 v69, 0x42800000, v73
	v_mov_b32_e32 v141, v3
	v_cvt_pk_fp8_f32 v141, v68, v69
	v_mul_f32_e32 v76, 0x42800000, v125
	v_mul_f32_e32 v80, 0x42800000, v129
	v_cvt_pk_fp8_f32 v138, v76, v80 op_sel:[0,0,1]
	v_mul_f32_e32 v76, 0x42800000, v109
	v_mul_f32_e32 v80, 0x42800000, v113
	v_cvt_pk_fp8_f32 v139, v76, v80 op_sel:[0,0,1]
	v_mul_f32_e32 v76, 0x42800000, v93
	v_mul_f32_e32 v80, 0x42800000, v97
	v_mul_f32_e32 v72, 0x42800000, v77
	v_mul_f32_e32 v73, 0x42800000, v81
	v_cvt_pk_fp8_f32 v140, v76, v80 op_sel:[0,0,1]
	v_cvt_pk_fp8_f32 v141, v72, v73 op_sel:[0,0,1]
	v_or_b32_e32 v68, 1, v132
	v_ashrrev_i32_e32 v69, 31, v68
	v_lshlrev_b64 v[68:69], 10, v[68:69]
	v_lshl_add_u64 v[68:69], v[136:137], 0, v[68:69]
	global_store_dwordx4 v[68:69], v[138:141], off nt
	v_mul_f32_e32 v68, 0x42800000, v118
	v_mul_f32_e32 v69, 0x42800000, v122
	v_mov_b32_e32 v138, v3
	v_cvt_pk_fp8_f32 v138, v68, v69
	v_mul_f32_e32 v68, 0x42800000, v102
	v_mul_f32_e32 v69, 0x42800000, v106
	v_mov_b32_e32 v139, v3
	v_cvt_pk_fp8_f32 v139, v68, v69
	v_mul_f32_e32 v68, 0x42800000, v86
	v_mul_f32_e32 v69, 0x42800000, v90
	v_mov_b32_e32 v140, v3
	v_cvt_pk_fp8_f32 v140, v68, v69
	v_mul_f32_e32 v68, 0x42800000, v70
	v_mul_f32_e32 v69, 0x42800000, v74
	v_mov_b32_e32 v141, v3
	v_mul_f32_e32 v72, 0x42800000, v126
	v_mul_f32_e32 v73, 0x42800000, v130
	v_cvt_pk_fp8_f32 v141, v68, v69
	v_cvt_pk_fp8_f32 v138, v72, v73 op_sel:[0,0,1]
	v_mul_f32_e32 v72, 0x42800000, v110
	v_mul_f32_e32 v73, 0x42800000, v114
	v_cvt_pk_fp8_f32 v139, v72, v73 op_sel:[0,0,1]
	v_mul_f32_e32 v72, 0x42800000, v94
	v_mul_f32_e32 v73, 0x42800000, v98
	v_cvt_pk_fp8_f32 v140, v72, v73 op_sel:[0,0,1]
	v_mul_f32_e32 v70, 0x42800000, v78
	v_mul_f32_e32 v72, 0x42800000, v82
	v_cvt_pk_fp8_f32 v141, v70, v72 op_sel:[0,0,1]
	v_or_b32_e32 v68, 2, v132
	v_ashrrev_i32_e32 v69, 31, v68
	v_lshlrev_b64 v[68:69], 10, v[68:69]
	v_lshl_add_u64 v[68:69], v[136:137], 0, v[68:69]
	global_store_dwordx4 v[68:69], v[138:141], off nt
	v_mul_f32_e32 v69, 0x42800000, v119
	v_mul_f32_e32 v70, 0x42800000, v123
	v_mov_b32_e32 v68, v3
	v_cvt_pk_fp8_f32 v68, v69, v70
	v_mul_f32_e32 v72, 0x42800000, v127
	v_mul_f32_e32 v73, 0x42800000, v131
	v_mul_f32_e32 v70, 0x42800000, v103
	v_cvt_pk_fp8_f32 v68, v72, v73 op_sel:[0,0,1]
	v_mul_f32_e32 v72, 0x42800000, v107
	v_mov_b32_e32 v69, v3
	v_cvt_pk_fp8_f32 v69, v70, v72
	v_mul_f32_e32 v73, 0x42800000, v111
	v_mul_f32_e32 v74, 0x42800000, v115
	v_mul_f32_e32 v72, 0x42800000, v87
	v_cvt_pk_fp8_f32 v69, v73, v74 op_sel:[0,0,1]
	v_mul_f32_e32 v73, 0x42800000, v91
	v_mov_b32_e32 v70, v3
	v_cvt_pk_fp8_f32 v70, v72, v73
	v_mul_f32_e32 v72, 0x42800000, v71
	v_mul_f32_e32 v73, 0x42800000, v75
	v_mov_b32_e32 v71, v3
	v_cvt_pk_fp8_f32 v71, v72, v73
	v_mul_f32_e32 v74, 0x42800000, v95
	v_mul_f32_e32 v76, 0x42800000, v99
	v_cvt_pk_fp8_f32 v70, v74, v76 op_sel:[0,0,1]
	v_mul_f32_e32 v74, 0x42800000, v79
	v_mul_f32_e32 v75, 0x42800000, v83
	v_cvt_pk_fp8_f32 v71, v74, v75 op_sel:[0,0,1]
	v_or_b32_e32 v72, 3, v132
	v_ashrrev_i32_e32 v73, 31, v72
	v_lshlrev_b64 v[72:73], 10, v[72:73]
	v_lshl_add_u64 v[72:73], v[136:137], 0, v[72:73]
	global_store_dwordx4 v[72:73], v[68:71], off nt
	s_waitcnt vmcnt(19)
	v_mul_f32_e32 v52, 0x42800000, v52
	s_waitcnt vmcnt(18)
	v_mul_f32_e32 v56, 0x42800000, v56
	v_mov_b32_e32 v70, v3
	s_waitcnt vmcnt(15)
	v_mul_f32_e32 v36, 0x42800000, v36
	s_waitcnt vmcnt(14)
	v_mul_f32_e32 v40, 0x42800000, v40
	v_mov_b32_e32 v71, v3
	s_waitcnt vmcnt(11)
	v_mul_f32_e32 v20, 0x42800000, v20
	s_waitcnt vmcnt(10)
	v_mul_f32_e32 v24, 0x42800000, v24
	v_mov_b32_e32 v72, v3
	s_waitcnt vmcnt(7)
	v_mul_f32_e32 v4, 0x42800000, v4
	s_waitcnt vmcnt(6)
	v_mul_f32_e32 v8, 0x42800000, v8
	v_mov_b32_e32 v73, v3
	v_cvt_pk_fp8_f32 v70, v52, v56
	v_cvt_pk_fp8_f32 v71, v36, v40
	v_cvt_pk_fp8_f32 v72, v20, v24
	v_cvt_pk_fp8_f32 v73, v4, v8
	v_mul_f32_e32 v60, 0x42800000, v60
	v_mul_f32_e32 v64, 0x42800000, v64
	v_mul_f32_e32 v44, 0x42800000, v44
	v_mul_f32_e32 v48, 0x42800000, v48
	v_mul_f32_e32 v28, 0x42800000, v28
	v_mul_f32_e32 v32, 0x42800000, v32
	s_waitcnt vmcnt(5)
	v_mul_f32_e32 v12, 0x42800000, v12
	s_waitcnt vmcnt(4)
	v_mul_f32_e32 v16, 0x42800000, v16
	v_or_b32_e32 v68, s17, v134
	v_cvt_pk_fp8_f32 v70, v60, v64 op_sel:[0,0,1]
	v_cvt_pk_fp8_f32 v71, v44, v48 op_sel:[0,0,1]
	v_cvt_pk_fp8_f32 v72, v28, v32 op_sel:[0,0,1]
	v_cvt_pk_fp8_f32 v73, v12, v16 op_sel:[0,0,1]
	v_ashrrev_i32_e32 v69, 31, v68
	v_lshlrev_b64 v[74:75], 10, v[68:69]
	v_lshl_add_u64 v[74:75], v[136:137], 0, v[74:75]
	global_store_dwordx4 v[74:75], v[70:73], off nt
	v_mul_f32_e32 v4, 0x42800000, v53
	v_mul_f32_e32 v8, 0x42800000, v57
	v_mov_b32_e32 v70, v3
	v_cvt_pk_fp8_f32 v70, v4, v8
	v_mul_f32_e32 v4, 0x42800000, v37
	v_mul_f32_e32 v8, 0x42800000, v41
	v_mov_b32_e32 v71, v3
	v_cvt_pk_fp8_f32 v71, v4, v8
	v_mul_f32_e32 v4, 0x42800000, v21
	v_mul_f32_e32 v8, 0x42800000, v25
	v_mov_b32_e32 v72, v3
	v_cvt_pk_fp8_f32 v72, v4, v8
	v_mul_f32_e32 v4, 0x42800000, v5
	v_mul_f32_e32 v5, 0x42800000, v9
	v_mov_b32_e32 v73, v3
	v_cvt_pk_fp8_f32 v73, v4, v5
	v_mul_f32_e32 v12, 0x42800000, v61
	v_mul_f32_e32 v16, 0x42800000, v65
	v_cvt_pk_fp8_f32 v70, v12, v16 op_sel:[0,0,1]
	v_mul_f32_e32 v12, 0x42800000, v45
	v_mul_f32_e32 v16, 0x42800000, v49
	v_cvt_pk_fp8_f32 v71, v12, v16 op_sel:[0,0,1]
	v_mul_f32_e32 v12, 0x42800000, v29
	v_mul_f32_e32 v16, 0x42800000, v33
	v_mul_f32_e32 v8, 0x42800000, v13
	v_mul_f32_e32 v9, 0x42800000, v17
	v_cvt_pk_fp8_f32 v72, v12, v16 op_sel:[0,0,1]
	v_cvt_pk_fp8_f32 v73, v8, v9 op_sel:[0,0,1]
	v_or_b32_e32 v4, 1, v68
	v_ashrrev_i32_e32 v5, 31, v4
	v_lshlrev_b64 v[4:5], 10, v[4:5]
	v_lshl_add_u64 v[4:5], v[136:137], 0, v[4:5]
	global_store_dwordx4 v[4:5], v[70:73], off nt
	v_mul_f32_e32 v4, 0x42800000, v54
	v_mul_f32_e32 v5, 0x42800000, v58
	v_mov_b32_e32 v70, v3
	v_cvt_pk_fp8_f32 v70, v4, v5
	v_mul_f32_e32 v4, 0x42800000, v38
	v_mul_f32_e32 v5, 0x42800000, v42
	v_mov_b32_e32 v71, v3
	v_cvt_pk_fp8_f32 v71, v4, v5
	v_mul_f32_e32 v4, 0x42800000, v22
	v_mul_f32_e32 v5, 0x42800000, v26
	v_mov_b32_e32 v72, v3
	v_cvt_pk_fp8_f32 v72, v4, v5
	v_mul_f32_e32 v4, 0x42800000, v6
	v_mul_f32_e32 v5, 0x42800000, v10
	v_mov_b32_e32 v73, v3
	v_mul_f32_e32 v8, 0x42800000, v62
	v_mul_f32_e32 v9, 0x42800000, v66
	v_cvt_pk_fp8_f32 v73, v4, v5
	v_cvt_pk_fp8_f32 v70, v8, v9 op_sel:[0,0,1]
	v_mul_f32_e32 v8, 0x42800000, v46
	v_mul_f32_e32 v9, 0x42800000, v50
	v_cvt_pk_fp8_f32 v71, v8, v9 op_sel:[0,0,1]
	v_mul_f32_e32 v8, 0x42800000, v30
	v_mul_f32_e32 v9, 0x42800000, v34
	v_cvt_pk_fp8_f32 v72, v8, v9 op_sel:[0,0,1]
	v_mul_f32_e32 v6, 0x42800000, v14
	v_mul_f32_e32 v8, 0x42800000, v18
	v_cvt_pk_fp8_f32 v73, v6, v8 op_sel:[0,0,1]
	v_or_b32_e32 v4, 2, v68
	v_ashrrev_i32_e32 v5, 31, v4
	v_lshlrev_b64 v[4:5], 10, v[4:5]
	v_lshl_add_u64 v[4:5], v[136:137], 0, v[4:5]
	global_store_dwordx4 v[4:5], v[70:73], off nt
	v_mul_f32_e32 v5, 0x42800000, v55
	v_mul_f32_e32 v6, 0x42800000, v59
	v_mov_b32_e32 v4, v3
	v_cvt_pk_fp8_f32 v4, v5, v6
	v_mul_f32_e32 v8, 0x42800000, v63
	v_mul_f32_e32 v9, 0x42800000, v67
	v_mul_f32_e32 v6, 0x42800000, v39
	v_cvt_pk_fp8_f32 v4, v8, v9 op_sel:[0,0,1]
	v_mul_f32_e32 v8, 0x42800000, v43
	v_mov_b32_e32 v5, v3
	v_cvt_pk_fp8_f32 v5, v6, v8
	v_mul_f32_e32 v9, 0x42800000, v47
	v_mul_f32_e32 v10, 0x42800000, v51
	v_mul_f32_e32 v8, 0x42800000, v23
	v_cvt_pk_fp8_f32 v5, v9, v10 op_sel:[0,0,1]
	v_mul_f32_e32 v9, 0x42800000, v27
	v_mov_b32_e32 v6, v3
	v_cvt_pk_fp8_f32 v6, v8, v9
	v_mul_f32_e32 v8, 0x42800000, v7
	v_mul_f32_e32 v9, 0x42800000, v11
	v_mov_b32_e32 v7, v3
	v_cvt_pk_fp8_f32 v7, v8, v9
	v_mul_f32_e32 v10, 0x42800000, v31
	v_mul_f32_e32 v12, 0x42800000, v35
	v_cvt_pk_fp8_f32 v6, v10, v12 op_sel:[0,0,1]
	v_mul_f32_e32 v10, 0x42800000, v15
	v_mul_f32_e32 v11, 0x42800000, v19
	v_cvt_pk_fp8_f32 v7, v10, v11 op_sel:[0,0,1]
	v_or_b32_e32 v8, 3, v68
	s_mov_b64 s[16:17], 0

.LBB0_1397:
	s_or_b64 exec, exec, s[4:5]
	s_waitcnt lgkmcnt(0)
	s_barrier
	ds_read_b32 v2, v1
	s_mov_b64 s[4:5], -1
	s_waitcnt lgkmcnt(0)
	v_readfirstlane_b32 s2, v2
	s_cmp_gt_i32 s2, 127
	s_cbranch_scc1 .LBB0_1392
	s_lshr_b32 s3, s2, 31
	s_mov_b64 s[20:21], s[44:45]
	v_mov_b32_e32 v2, v0
	s_add_i32 s3, s2, s3
	s_load_dwordx2 s[18:19], s[20:21], 0xd8
	s_ashr_i32 s16, s3, 2
	s_and_b32 s3, s3, -4
	s_sub_i32 s4, s2, s3
	v_readfirstlane_b32 s3, v2
	s_add_i32 s2, s4, 32
	s_ashr_i32 s3, s3, 6
	v_lshlrev_b32_e32 v3, 1, v2
	v_lshlrev_b32_e32 v2, 2, v2
	s_cmp_gt_i32 s4, -1
	v_and_b32_e32 v130, 0x70, v3
	v_and_b32_e32 v134, 28, v2
	s_mov_b64 s[4:5], -1
	s_cbranch_scc0 .LBB0_1400
	s_lshl_b32 s4, s2, 6
	s_add_i32 s4, s4, 0x7ffff800
	s_and_b32 s41, s4, 0x7fffff80
	s_lshl_b32 s4, s2, 10
	s_and_b32 s17, s4, 0x400
	s_load_dwordx2 s[4:5], s[20:21], 0xc8
	s_lshl_b32 s22, s3, 7
	s_add_i32 s22, s22, s17
	s_ashr_i32 s17, s16, 31
	s_lshl_b64 s[24:25], s[16:17], 23
	v_lshlrev_b32_e32 v135, 11, v130
	s_waitcnt lgkmcnt(0)
	s_add_u32 s4, s4, s24
	v_add_u32_e32 v2, s22, v135
	s_addc_u32 s5, s5, s25
	v_or_b32_e32 v2, v2, v134
	s_and_b32 s5, s5, 0xffff
	v_lshlrev_b32_e32 v34, 2, v2
	s_lshl_b32 s26, s41, 13
	s_or_b32 s27, s26, 0x2000
	buffer_load_dwordx4 v[2:5], v34, s[4:7], s26 offen nt
	buffer_load_dwordx4 v[6:9], v34, s[4:7], s27 offen nt
	s_or_b32 s29, s26, 0x4000
	s_or_b32 s31, s26, 0x8000
	s_or_b32 s23, s26, 0xc000
	s_or_b32 s28, s26, 0x10000
	s_or_b32 s33, s26, 0x12000
	s_or_b32 s30, s26, 0x6000
	buffer_load_dwordx4 v[10:13], v34, s[4:7], s29 offen nt
	buffer_load_dwordx4 v[14:17], v34, s[4:7], s30 offen nt
	s_or_b32 s25, s26, 0xa000
	buffer_load_dwordx4 v[18:21], v34, s[4:7], s31 offen nt
	buffer_load_dwordx4 v[22:25], v34, s[4:7], s25 offen nt
	s_or_b32 s24, s26, 0xe000
	buffer_load_dwordx4 v[26:29], v34, s[4:7], s23 offen nt
	buffer_load_dwordx4 v[30:33], v34, s[4:7], s24 offen nt
	buffer_load_dwordx4 v[42:45], v34, s[4:7], s28 offen nt
	buffer_load_dwordx4 v[46:49], v34, s[4:7], s33 offen nt
	s_or_b32 s34, s26, 0x14000
	s_or_b32 s36, s26, 0x16000
	s_or_b32 s35, s26, 0x18000
	buffer_load_dwordx4 v[58:61], v34, s[4:7], s34 offen nt
	buffer_load_dwordx4 v[62:65], v34, s[4:7], s36 offen nt
	s_or_b32 s39, s26, 0x1a000
	buffer_load_dwordx4 v[82:85], v34, s[4:7], s35 offen nt
	buffer_load_dwordx4 v[86:89], v34, s[4:7], s39 offen nt
	s_or_b32 s37, s26, 0x1c000
	s_or_b32 s38, s26, 0x1e000
	buffer_load_dwordx4 v[90:93], v34, s[4:7], s37 offen nt
	buffer_load_dwordx4 v[94:97], v34, s[4:7], s38 offen nt
	s_or_b32 s40, s22, 32
	v_add_u32_e32 v34, s40, v135
	v_or_b32_e32 v34, v34, v134
	v_lshlrev_b32_e32 v38, 2, v34
	buffer_load_dwordx4 v[114:117], v38, s[4:7], s26 offen nt
	buffer_load_dwordx4 v[118:121], v38, s[4:7], s27 offen nt
	buffer_load_dwordx4 v[122:125], v38, s[4:7], s29 offen nt
	buffer_load_dwordx4 v[126:129], v38, s[4:7], s30 offen nt
	buffer_load_dwordx4 v[106:109], v38, s[4:7], s31 offen nt
	buffer_load_dwordx4 v[110:113], v38, s[4:7], s25 offen nt
	buffer_load_dwordx4 v[98:101], v38, s[4:7], s23 offen nt
	buffer_load_dwordx4 v[102:105], v38, s[4:7], s24 offen nt
	buffer_load_dwordx4 v[66:69], v38, s[4:7], s28 offen nt
	buffer_load_dwordx4 v[70:73], v38, s[4:7], s33 offen nt
	buffer_load_dwordx4 v[74:77], v38, s[4:7], s34 offen nt
	buffer_load_dwordx4 v[78:81], v38, s[4:7], s36 offen nt
	buffer_load_dwordx4 v[50:53], v38, s[4:7], s35 offen nt
	buffer_load_dwordx4 v[54:57], v38, s[4:7], s39 offen nt
	buffer_load_dwordx4 v[34:37], v38, s[4:7], s37 offen nt
	s_nop 0
	buffer_load_dwordx4 v[38:41], v38, s[4:7], s38 offen nt
	v_mov_b32_e32 v136, v131
	v_mov_b32_e32 v138, v131
	v_mov_b32_e32 v137, v131
	v_mov_b32_e32 v139, v131
	s_lshl_b64 s[42:43], s[16:17], 21
	s_add_u32 s17, s18, s42
	s_addc_u32 s43, s19, s43
	s_add_u32 s42, s17, s41
	v_or_b32_e32 v140, s22, v134
	s_addc_u32 s43, s43, 0
	v_lshl_add_u64 v[132:133], s[42:43], 0, v[130:131]
	v_ashrrev_i32_e32 v141, 31, v140
	v_lshl_add_u64 v[132:133], v[132:133], 0, s[12:13]
	v_lshlrev_b64 v[142:143], 10, v[140:141]
	v_lshl_add_u64 v[142:143], v[132:133], 0, v[142:143]
	s_or_b32 s17, s22, 64
	s_or_b32 s22, s22, 0x60
	s_waitcnt vmcnt(31)
	v_mul_f32_e32 v2, 0x42800000, v2
	s_waitcnt vmcnt(30)
	v_mul_f32_e32 v6, 0x42800000, v6
	v_cvt_pk_fp8_f32 v136, v2, v6
	s_waitcnt vmcnt(29)
	v_mul_f32_e32 v10, 0x42800000, v10
	s_waitcnt vmcnt(28)
	v_mul_f32_e32 v14, 0x42800000, v14
	s_waitcnt vmcnt(27)
	v_mul_f32_e32 v18, 0x42800000, v18
	s_waitcnt vmcnt(26)
	v_mul_f32_e32 v22, 0x42800000, v22
	v_cvt_pk_fp8_f32 v136, v10, v14 op_sel:[0,0,1]
	v_cvt_pk_fp8_f32 v137, v18, v22
	s_waitcnt vmcnt(23)
	v_mul_f32_e32 v42, 0x42800000, v42
	s_waitcnt vmcnt(22)
	v_mul_f32_e32 v2, 0x42800000, v46
	v_cvt_pk_fp8_f32 v138, v42, v2
	v_mul_f32_e32 v26, 0x42800000, v26
	v_mul_f32_e32 v30, 0x42800000, v30
	s_waitcnt vmcnt(21)
	v_mul_f32_e32 v6, 0x42800000, v58
	s_waitcnt vmcnt(20)
	v_mul_f32_e32 v10, 0x42800000, v62
	s_waitcnt vmcnt(19)
	v_mul_f32_e32 v2, 0x42800000, v82
	s_waitcnt vmcnt(18)
	v_mul_f32_e32 v14, 0x42800000, v86
	v_cvt_pk_fp8_f32 v139, v2, v14
	v_cvt_pk_fp8_f32 v138, v6, v10 op_sel:[0,0,1]
	s_waitcnt vmcnt(17)
	v_mul_f32_e32 v2, 0x42800000, v90
	s_waitcnt vmcnt(16)
	v_mul_f32_e32 v6, 0x42800000, v94
	v_cvt_pk_fp8_f32 v137, v26, v30 op_sel:[0,0,1]
	v_cvt_pk_fp8_f32 v139, v2, v6 op_sel:[0,0,1]
	v_mul_f32_e32 v2, 0x42800000, v3
	v_mul_f32_e32 v3, 0x42800000, v7
	v_mul_f32_e32 v6, 0x42800000, v11
	global_store_dwordx4 v[142:143], v[136:139], off nt
	v_mul_f32_e32 v7, 0x42800000, v15
	s_waitcnt vmcnt(16)
	v_mul_f32_e32 v114, 0x42800000, v114
	v_mov_b32_e32 v136, v131
	v_cvt_pk_fp8_f32 v136, v2, v3
	v_mul_f32_e32 v2, 0x42800000, v19
	v_mul_f32_e32 v3, 0x42800000, v23
	v_mov_b32_e32 v137, v131
	v_cvt_pk_fp8_f32 v137, v2, v3
	v_mul_f32_e32 v2, 0x42800000, v27
	v_mul_f32_e32 v3, 0x42800000, v31
	v_mov_b32_e32 v138, v131
	v_cvt_pk_fp8_f32 v137, v2, v3 op_sel:[0,0,1]
	v_mul_f32_e32 v2, 0x42800000, v43
	v_mul_f32_e32 v3, 0x42800000, v47
	v_cvt_pk_fp8_f32 v138, v2, v3
	v_mul_f32_e32 v2, 0x42800000, v83
	v_mul_f32_e32 v3, 0x42800000, v87
	v_mov_b32_e32 v139, v131
	v_cvt_pk_fp8_f32 v139, v2, v3
	v_cvt_pk_fp8_f32 v136, v6, v7 op_sel:[0,0,1]
	v_mul_f32_e32 v6, 0x42800000, v59
	v_mul_f32_e32 v7, 0x42800000, v63
	v_mul_f32_e32 v2, 0x42800000, v91
	v_mul_f32_e32 v3, 0x42800000, v95
	v_cvt_pk_fp8_f32 v138, v6, v7 op_sel:[0,0,1]
	v_cvt_pk_fp8_f32 v139, v2, v3 op_sel:[0,0,1]
	v_or_b32_e32 v2, 1, v140
	v_ashrrev_i32_e32 v3, 31, v2
	v_lshlrev_b64 v[2:3], 10, v[2:3]
	v_lshl_add_u64 v[2:3], v[132:133], 0, v[2:3]
	global_store_dwordx4 v[2:3], v[136:139], off nt
	v_mul_f32_e32 v2, 0x42800000, v4
	v_mul_f32_e32 v3, 0x42800000, v8
	v_mov_b32_e32 v136, v131
	v_cvt_pk_fp8_f32 v136, v2, v3
	v_mul_f32_e32 v2, 0x42800000, v20
	v_mul_f32_e32 v3, 0x42800000, v24
	v_mov_b32_e32 v137, v131
	v_cvt_pk_fp8_f32 v137, v2, v3
	v_mul_f32_e32 v2, 0x42800000, v28
	v_mul_f32_e32 v3, 0x42800000, v32
	v_mov_b32_e32 v138, v131
	v_cvt_pk_fp8_f32 v137, v2, v3 op_sel:[0,0,1]
	v_mul_f32_e32 v2, 0x42800000, v44
	v_mul_f32_e32 v3, 0x42800000, v48
	v_cvt_pk_fp8_f32 v138, v2, v3
	v_mul_f32_e32 v2, 0x42800000, v84
	v_mul_f32_e32 v3, 0x42800000, v88
	v_mov_b32_e32 v139, v131
	v_cvt_pk_fp8_f32 v139, v2, v3
	v_mul_f32_e32 v4, 0x42800000, v12
	v_mul_f32_e32 v6, 0x42800000, v16
	v_cvt_pk_fp8_f32 v136, v4, v6 op_sel:[0,0,1]
	v_mul_f32_e32 v4, 0x42800000, v60
	v_mul_f32_e32 v6, 0x42800000, v64
	v_mul_f32_e32 v2, 0x42800000, v92
	v_mul_f32_e32 v3, 0x42800000, v96
	v_cvt_pk_fp8_f32 v138, v4, v6 op_sel:[0,0,1]
	v_cvt_pk_fp8_f32 v139, v2, v3 op_sel:[0,0,1]
	v_or_b32_e32 v2, 2, v140
	v_ashrrev_i32_e32 v3, 31, v2
	v_lshlrev_b64 v[2:3], 10, v[2:3]
	v_lshl_add_u64 v[2:3], v[132:133], 0, v[2:3]
	global_store_dwordx4 v[2:3], v[136:139], off nt
	v_mul_f32_e32 v3, 0x42800000, v5
	v_mul_f32_e32 v4, 0x42800000, v9
	v_mov_b32_e32 v2, v131
	v_cvt_pk_fp8_f32 v2, v3, v4
	v_mul_f32_e32 v4, 0x42800000, v21
	v_mul_f32_e32 v7, 0x42800000, v25
	v_mov_b32_e32 v3, v131
	v_cvt_pk_fp8_f32 v3, v4, v7
	v_mul_f32_e32 v5, 0x42800000, v13
	v_mul_f32_e32 v6, 0x42800000, v17
	v_cvt_pk_fp8_f32 v2, v5, v6 op_sel:[0,0,1]
	v_mul_f32_e32 v4, 0x42800000, v29
	v_mul_f32_e32 v5, 0x42800000, v33
	v_cvt_pk_fp8_f32 v3, v4, v5 op_sel:[0,0,1]
	v_mul_f32_e32 v5, 0x42800000, v45
	v_mul_f32_e32 v6, 0x42800000, v49
	v_mov_b32_e32 v4, v131
	v_cvt_pk_fp8_f32 v4, v5, v6
	v_mul_f32_e32 v6, 0x42800000, v85
	v_mul_f32_e32 v9, 0x42800000, v89
	v_mov_b32_e32 v5, v131
	v_cvt_pk_fp8_f32 v5, v6, v9
	v_mul_f32_e32 v7, 0x42800000, v61
	v_mul_f32_e32 v8, 0x42800000, v65
	v_cvt_pk_fp8_f32 v4, v7, v8 op_sel:[0,0,1]
	v_mul_f32_e32 v6, 0x42800000, v93
	v_mul_f32_e32 v7, 0x42800000, v97
	v_cvt_pk_fp8_f32 v5, v6, v7 op_sel:[0,0,1]
	v_or_b32_e32 v6, 3, v140
	v_ashrrev_i32_e32 v7, 31, v6
	v_lshlrev_b64 v[6:7], 10, v[6:7]
	v_lshl_add_u64 v[6:7], v[132:133], 0, v[6:7]
	global_store_dwordx4 v[6:7], v[2:5], off nt
	s_waitcnt vmcnt(18)
	v_mul_f32_e32 v118, 0x42800000, v118
	v_mov_b32_e32 v136, v131
	v_add_u32_e32 v2, s17, v135
	v_or_b32_e32 v2, v2, v134
	v_lshlrev_b32_e32 v6, 2, v2
	buffer_load_dwordx4 v[82:85], v6, s[4:7], s26 offen nt
	buffer_load_dwordx4 v[86:89], v6, s[4:7], s27 offen nt
	buffer_load_dwordx4 v[90:93], v6, s[4:7], s29 offen nt
	buffer_load_dwordx4 v[94:97], v6, s[4:7], s30 offen nt
	buffer_load_dwordx4 v[58:61], v6, s[4:7], s31 offen nt
	buffer_load_dwordx4 v[62:65], v6, s[4:7], s25 offen nt
	buffer_load_dwordx4 v[42:45], v6, s[4:7], s23 offen nt
	buffer_load_dwordx4 v[46:49], v6, s[4:7], s24 offen nt
	buffer_load_dwordx4 v[18:21], v6, s[4:7], s28 offen nt
	buffer_load_dwordx4 v[22:25], v6, s[4:7], s33 offen nt
	buffer_load_dwordx4 v[26:29], v6, s[4:7], s34 offen nt
	buffer_load_dwordx4 v[30:33], v6, s[4:7], s36 offen nt
	buffer_load_dwordx4 v[10:13], v6, s[4:7], s35 offen nt
	buffer_load_dwordx4 v[14:17], v6, s[4:7], s39 offen nt
	buffer_load_dwordx4 v[2:5], v6, s[4:7], s37 offen nt
	s_nop 0
	buffer_load_dwordx4 v[6:9], v6, s[4:7], s38 offen nt
	s_waitcnt vmcnt(31)
	v_mul_f32_e32 v106, 0x42800000, v106
	s_waitcnt vmcnt(30)
	v_mul_f32_e32 v110, 0x42800000, v110
	v_mov_b32_e32 v137, v131
	s_waitcnt vmcnt(27)
	v_mul_f32_e32 v66, 0x42800000, v66
	s_waitcnt vmcnt(26)
	v_mul_f32_e32 v70, 0x42800000, v70
	v_mov_b32_e32 v138, v131
	s_waitcnt vmcnt(23)
	v_mul_f32_e32 v50, 0x42800000, v50
	s_waitcnt vmcnt(22)
	v_mul_f32_e32 v54, 0x42800000, v54
	v_mov_b32_e32 v139, v131
	v_cvt_pk_fp8_f32 v136, v114, v118
	v_cvt_pk_fp8_f32 v137, v106, v110
	v_cvt_pk_fp8_f32 v138, v66, v70
	v_cvt_pk_fp8_f32 v139, v50, v54
	v_mul_f32_e32 v122, 0x42800000, v122
	v_mul_f32_e32 v126, 0x42800000, v126
	v_mul_f32_e32 v98, 0x42800000, v98
	v_mul_f32_e32 v102, 0x42800000, v102
	v_mul_f32_e32 v74, 0x42800000, v74
	v_mul_f32_e32 v78, 0x42800000, v78
	s_waitcnt vmcnt(21)
	v_mul_f32_e32 v34, 0x42800000, v34
	s_waitcnt vmcnt(20)
	v_mul_f32_e32 v38, 0x42800000, v38
	v_or_b32_e32 v140, s40, v134
	v_cvt_pk_fp8_f32 v136, v122, v126 op_sel:[0,0,1]
	v_cvt_pk_fp8_f32 v137, v98, v102 op_sel:[0,0,1]
	v_cvt_pk_fp8_f32 v138, v74, v78 op_sel:[0,0,1]
	v_cvt_pk_fp8_f32 v139, v34, v38 op_sel:[0,0,1]
	v_ashrrev_i32_e32 v141, 31, v140
	v_lshlrev_b64 v[142:143], 10, v[140:141]
	v_lshl_add_u64 v[142:143], v[132:133], 0, v[142:143]
	global_store_dwordx4 v[142:143], v[136:139], off nt
	v_mul_f32_e32 v34, 0x42800000, v115
	v_mul_f32_e32 v38, 0x42800000, v119
	v_mov_b32_e32 v136, v131
	v_cvt_pk_fp8_f32 v136, v34, v38
	v_mul_f32_e32 v34, 0x42800000, v107
	v_mul_f32_e32 v38, 0x42800000, v111
	v_mov_b32_e32 v137, v131
	v_cvt_pk_fp8_f32 v137, v34, v38
	v_mul_f32_e32 v34, 0x42800000, v99
	v_mul_f32_e32 v38, 0x42800000, v103
	v_mov_b32_e32 v138, v131
	v_cvt_pk_fp8_f32 v137, v34, v38 op_sel:[0,0,1]
	v_mul_f32_e32 v34, 0x42800000, v67
	v_mul_f32_e32 v38, 0x42800000, v71
	v_cvt_pk_fp8_f32 v138, v34, v38
	v_mul_f32_e32 v34, 0x42800000, v51
	v_mul_f32_e32 v38, 0x42800000, v55
	v_mov_b32_e32 v139, v131
	v_cvt_pk_fp8_f32 v139, v34, v38
	v_mul_f32_e32 v50, 0x42800000, v123
	v_mul_f32_e32 v54, 0x42800000, v127
	v_cvt_pk_fp8_f32 v136, v50, v54 op_sel:[0,0,1]
	v_mul_f32_e32 v50, 0x42800000, v75
	v_mul_f32_e32 v54, 0x42800000, v79
	v_mul_f32_e32 v34, 0x42800000, v35
	v_mul_f32_e32 v35, 0x42800000, v39
	v_cvt_pk_fp8_f32 v138, v50, v54 op_sel:[0,0,1]
	v_cvt_pk_fp8_f32 v139, v34, v35 op_sel:[0,0,1]
	v_or_b32_e32 v34, 1, v140
	v_ashrrev_i32_e32 v35, 31, v34
	v_lshlrev_b64 v[34:35], 10, v[34:35]
	v_lshl_add_u64 v[34:35], v[132:133], 0, v[34:35]
	global_store_dwordx4 v[34:35], v[136:139], off nt
	v_mul_f32_e32 v34, 0x42800000, v116
	v_mul_f32_e32 v35, 0x42800000, v120
	v_mov_b32_e32 v136, v131
	v_cvt_pk_fp8_f32 v136, v34, v35
	v_mul_f32_e32 v34, 0x42800000, v108
	v_mul_f32_e32 v35, 0x42800000, v112
	v_mov_b32_e32 v137, v131
	v_cvt_pk_fp8_f32 v137, v34, v35
	v_mul_f32_e32 v34, 0x42800000, v100
	v_mul_f32_e32 v35, 0x42800000, v104
	v_mov_b32_e32 v138, v131
	v_cvt_pk_fp8_f32 v137, v34, v35 op_sel:[0,0,1]
	v_mul_f32_e32 v34, 0x42800000, v68
	v_mul_f32_e32 v35, 0x42800000, v72
	v_cvt_pk_fp8_f32 v138, v34, v35
	v_mul_f32_e32 v34, 0x42800000, v52
	v_mul_f32_e32 v35, 0x42800000, v56
	v_mov_b32_e32 v139, v131
	v_cvt_pk_fp8_f32 v139, v34, v35
	v_mul_f32_e32 v38, 0x42800000, v124
	v_mul_f32_e32 v39, 0x42800000, v128
	v_cvt_pk_fp8_f32 v136, v38, v39 op_sel:[0,0,1]
	v_mul_f32_e32 v38, 0x42800000, v76
	v_mul_f32_e32 v39, 0x42800000, v80
	v_mul_f32_e32 v34, 0x42800000, v36
	v_mul_f32_e32 v35, 0x42800000, v40
	v_cvt_pk_fp8_f32 v138, v38, v39 op_sel:[0,0,1]
	v_cvt_pk_fp8_f32 v139, v34, v35 op_sel:[0,0,1]
	v_or_b32_e32 v34, 2, v140
	v_ashrrev_i32_e32 v35, 31, v34
	v_lshlrev_b64 v[34:35], 10, v[34:35]
	v_lshl_add_u64 v[34:35], v[132:133], 0, v[34:35]
	global_store_dwordx4 v[34:35], v[136:139], off nt
	v_mul_f32_e32 v34, 0x42800000, v117
	v_mul_f32_e32 v35, 0x42800000, v121
	v_mov_b32_e32 v50, v131
	v_cvt_pk_fp8_f32 v50, v34, v35
	v_mul_f32_e32 v34, 0x42800000, v109
	v_mul_f32_e32 v35, 0x42800000, v113
	v_mov_b32_e32 v51, v131
	v_cvt_pk_fp8_f32 v51, v34, v35
	v_mul_f32_e32 v34, 0x42800000, v101
	v_mul_f32_e32 v35, 0x42800000, v105
	v_mov_b32_e32 v52, v131
	v_cvt_pk_fp8_f32 v51, v34, v35 op_sel:[0,0,1]
	v_mul_f32_e32 v34, 0x42800000, v69
	v_mul_f32_e32 v35, 0x42800000, v73
	v_cvt_pk_fp8_f32 v52, v34, v35
	v_mul_f32_e32 v34, 0x42800000, v53
	v_mul_f32_e32 v35, 0x42800000, v57
	v_mov_b32_e32 v53, v131
	v_cvt_pk_fp8_f32 v53, v34, v35
	v_mul_f32_e32 v36, 0x42800000, v125
	v_mul_f32_e32 v38, 0x42800000, v129
	v_cvt_pk_fp8_f32 v50, v36, v38 op_sel:[0,0,1]
	v_mul_f32_e32 v36, 0x42800000, v77
	v_mul_f32_e32 v38, 0x42800000, v81
	v_mul_f32_e32 v34, 0x42800000, v37
	v_mul_f32_e32 v35, 0x42800000, v41
	v_cvt_pk_fp8_f32 v52, v36, v38 op_sel:[0,0,1]
	v_cvt_pk_fp8_f32 v53, v34, v35 op_sel:[0,0,1]
	v_or_b32_e32 v34, 3, v140
	v_ashrrev_i32_e32 v35, 31, v34
	v_lshlrev_b64 v[34:35], 10, v[34:35]
	v_lshl_add_u64 v[34:35], v[132:133], 0, v[34:35]
	global_store_dwordx4 v[34:35], v[50:53], off nt
	v_add_u32_e32 v34, s22, v135
	v_or_b32_e32 v34, v34, v134
	v_lshlrev_b32_e32 v78, 2, v34
	buffer_load_dwordx4 v[114:117], v78, s[4:7], s26 offen nt
	buffer_load_dwordx4 v[118:121], v78, s[4:7], s27 offen nt
	buffer_load_dwordx4 v[122:125], v78, s[4:7], s29 offen nt
	buffer_load_dwordx4 v[126:129], v78, s[4:7], s30 offen nt
	buffer_load_dwordx4 v[106:109], v78, s[4:7], s31 offen nt
	buffer_load_dwordx4 v[110:113], v78, s[4:7], s25 offen nt
	buffer_load_dwordx4 v[98:101], v78, s[4:7], s23 offen nt
	buffer_load_dwordx4 v[102:105], v78, s[4:7], s24 offen nt
	buffer_load_dwordx4 v[50:53], v78, s[4:7], s28 offen nt
	buffer_load_dwordx4 v[54:57], v78, s[4:7], s33 offen nt
	buffer_load_dwordx4 v[66:69], v78, s[4:7], s34 offen nt
	buffer_load_dwordx4 v[70:73], v78, s[4:7], s36 offen nt
	buffer_load_dwordx4 v[34:37], v78, s[4:7], s35 offen nt
	buffer_load_dwordx4 v[38:41], v78, s[4:7], s39 offen nt
	buffer_load_dwordx4 v[74:77], v78, s[4:7], s37 offen nt
	s_nop 0
	buffer_load_dwordx4 v[78:81], v78, s[4:7], s38 offen nt
	s_waitcnt vmcnt(35)
	v_mul_f32_e32 v82, 0x42800000, v82
	s_waitcnt vmcnt(34)
	v_mul_f32_e32 v86, 0x42800000, v86
	v_mov_b32_e32 v136, v131
	s_waitcnt vmcnt(31)
	v_mul_f32_e32 v58, 0x42800000, v58
	s_waitcnt vmcnt(30)
	v_mul_f32_e32 v62, 0x42800000, v62
	v_mov_b32_e32 v137, v131
	s_waitcnt vmcnt(27)
	v_mul_f32_e32 v18, 0x42800000, v18
	s_waitcnt vmcnt(26)
	v_mul_f32_e32 v22, 0x42800000, v22
	v_mov_b32_e32 v138, v131
	s_waitcnt vmcnt(23)
	v_mul_f32_e32 v10, 0x42800000, v10
	s_waitcnt vmcnt(22)
	v_mul_f32_e32 v14, 0x42800000, v14
	v_mov_b32_e32 v139, v131
	v_cvt_pk_fp8_f32 v136, v82, v86
	v_cvt_pk_fp8_f32 v137, v58, v62
	v_cvt_pk_fp8_f32 v138, v18, v22
	v_cvt_pk_fp8_f32 v139, v10, v14
	v_mul_f32_e32 v90, 0x42800000, v90
	v_mul_f32_e32 v94, 0x42800000, v94
	v_mul_f32_e32 v42, 0x42800000, v42
	v_mul_f32_e32 v46, 0x42800000, v46
	v_mul_f32_e32 v26, 0x42800000, v26
	v_mul_f32_e32 v30, 0x42800000, v30
	s_waitcnt vmcnt(21)
	v_mul_f32_e32 v2, 0x42800000, v2
	s_waitcnt vmcnt(20)
	v_mul_f32_e32 v6, 0x42800000, v6
	v_or_b32_e32 v140, s17, v134
	v_cvt_pk_fp8_f32 v136, v90, v94 op_sel:[0,0,1]
	v_cvt_pk_fp8_f32 v137, v42, v46 op_sel:[0,0,1]
	v_cvt_pk_fp8_f32 v138, v26, v30 op_sel:[0,0,1]
	v_cvt_pk_fp8_f32 v139, v2, v6 op_sel:[0,0,1]
	v_ashrrev_i32_e32 v141, 31, v140
	v_lshlrev_b64 v[142:143], 10, v[140:141]
	v_lshl_add_u64 v[142:143], v[132:133], 0, v[142:143]
	global_store_dwordx4 v[142:143], v[136:139], off nt
	v_mul_f32_e32 v2, 0x42800000, v83
	v_mul_f32_e32 v6, 0x42800000, v87
	v_mov_b32_e32 v136, v131
	v_cvt_pk_fp8_f32 v136, v2, v6
	v_mul_f32_e32 v2, 0x42800000, v59
	v_mul_f32_e32 v6, 0x42800000, v63
	v_mov_b32_e32 v137, v131
	v_cvt_pk_fp8_f32 v137, v2, v6
	v_mul_f32_e32 v2, 0x42800000, v43
	v_mul_f32_e32 v6, 0x42800000, v47
	v_mov_b32_e32 v138, v131
	v_cvt_pk_fp8_f32 v137, v2, v6 op_sel:[0,0,1]
	v_mul_f32_e32 v2, 0x42800000, v19
	v_mul_f32_e32 v6, 0x42800000, v23
	v_cvt_pk_fp8_f32 v138, v2, v6
	v_mul_f32_e32 v2, 0x42800000, v11
	v_mul_f32_e32 v6, 0x42800000, v15
	v_mov_b32_e32 v139, v131
	v_cvt_pk_fp8_f32 v139, v2, v6
	v_mul_f32_e32 v10, 0x42800000, v91
	v_mul_f32_e32 v14, 0x42800000, v95
	v_cvt_pk_fp8_f32 v136, v10, v14 op_sel:[0,0,1]
	v_mul_f32_e32 v10, 0x42800000, v27
	v_mul_f32_e32 v14, 0x42800000, v31
	v_mul_f32_e32 v2, 0x42800000, v3
	v_mul_f32_e32 v3, 0x42800000, v7
	v_cvt_pk_fp8_f32 v138, v10, v14 op_sel:[0,0,1]
	v_cvt_pk_fp8_f32 v139, v2, v3 op_sel:[0,0,1]
	v_or_b32_e32 v2, 1, v140
	v_ashrrev_i32_e32 v3, 31, v2
	v_lshlrev_b64 v[2:3], 10, v[2:3]
	v_lshl_add_u64 v[2:3], v[132:133], 0, v[2:3]
	global_store_dwordx4 v[2:3], v[136:139], off nt
	v_mul_f32_e32 v2, 0x42800000, v84
	v_mul_f32_e32 v3, 0x42800000, v88
	v_mov_b32_e32 v136, v131
	v_cvt_pk_fp8_f32 v136, v2, v3
	v_mul_f32_e32 v2, 0x42800000, v60
	v_mul_f32_e32 v3, 0x42800000, v64
	v_mov_b32_e32 v137, v131
	v_cvt_pk_fp8_f32 v137, v2, v3
	v_mul_f32_e32 v2, 0x42800000, v44
	v_mul_f32_e32 v3, 0x42800000, v48
	v_mov_b32_e32 v138, v131
	v_cvt_pk_fp8_f32 v137, v2, v3 op_sel:[0,0,1]
	v_mul_f32_e32 v2, 0x42800000, v20
	v_mul_f32_e32 v3, 0x42800000, v24
	v_cvt_pk_fp8_f32 v138, v2, v3
	v_mul_f32_e32 v2, 0x42800000, v12
	v_mul_f32_e32 v3, 0x42800000, v16
	v_mov_b32_e32 v139, v131
	v_cvt_pk_fp8_f32 v139, v2, v3
	v_mul_f32_e32 v6, 0x42800000, v92
	v_mul_f32_e32 v7, 0x42800000, v96
	v_cvt_pk_fp8_f32 v136, v6, v7 op_sel:[0,0,1]
	v_mul_f32_e32 v6, 0x42800000, v28
	v_mul_f32_e32 v7, 0x42800000, v32
	v_mul_f32_e32 v2, 0x42800000, v4
	v_mul_f32_e32 v3, 0x42800000, v8
	v_cvt_pk_fp8_f32 v138, v6, v7 op_sel:[0,0,1]
	v_cvt_pk_fp8_f32 v139, v2, v3 op_sel:[0,0,1]
	v_or_b32_e32 v2, 2, v140
	v_ashrrev_i32_e32 v3, 31, v2
	v_lshlrev_b64 v[2:3], 10, v[2:3]
	v_lshl_add_u64 v[2:3], v[132:133], 0, v[2:3]
	global_store_dwordx4 v[2:3], v[136:139], off nt
	v_mul_f32_e32 v2, 0x42800000, v85
	v_mul_f32_e32 v3, 0x42800000, v89
	v_mov_b32_e32 v10, v131
	v_cvt_pk_fp8_f32 v10, v2, v3
	v_mul_f32_e32 v2, 0x42800000, v61
	v_mul_f32_e32 v3, 0x42800000, v65
	v_mov_b32_e32 v11, v131
	v_cvt_pk_fp8_f32 v11, v2, v3
	v_mul_f32_e32 v2, 0x42800000, v45
	v_mul_f32_e32 v3, 0x42800000, v49
	v_mov_b32_e32 v12, v131
	v_cvt_pk_fp8_f32 v11, v2, v3 op_sel:[0,0,1]
	v_mul_f32_e32 v2, 0x42800000, v21
	v_mul_f32_e32 v3, 0x42800000, v25
	v_cvt_pk_fp8_f32 v12, v2, v3
	v_mul_f32_e32 v2, 0x42800000, v13
	v_mul_f32_e32 v3, 0x42800000, v17
	v_mov_b32_e32 v13, v131
	v_cvt_pk_fp8_f32 v13, v2, v3
	v_mul_f32_e32 v4, 0x42800000, v93
	v_mul_f32_e32 v6, 0x42800000, v97
	v_cvt_pk_fp8_f32 v10, v4, v6 op_sel:[0,0,1]
	v_mul_f32_e32 v4, 0x42800000, v29
	v_mul_f32_e32 v6, 0x42800000, v33
	v_mul_f32_e32 v2, 0x42800000, v5
	v_mul_f32_e32 v3, 0x42800000, v9
	v_cvt_pk_fp8_f32 v12, v4, v6 op_sel:[0,0,1]
	v_cvt_pk_fp8_f32 v13, v2, v3 op_sel:[0,0,1]
	v_or_b32_e32 v2, 3, v140
	v_ashrrev_i32_e32 v3, 31, v2
	v_lshlrev_b64 v[2:3], 10, v[2:3]
	v_lshl_add_u64 v[2:3], v[132:133], 0, v[2:3]
	global_store_dwordx4 v[2:3], v[10:13], off nt
	s_waitcnt vmcnt(19)
	v_mul_f32_e32 v3, 0x42800000, v114
	s_waitcnt vmcnt(18)
	v_mul_f32_e32 v4, 0x42800000, v118
	v_mov_b32_e32 v2, v131
	v_cvt_pk_fp8_f32 v2, v3, v4
	s_waitcnt vmcnt(15)
	v_mul_f32_e32 v4, 0x42800000, v106
	s_waitcnt vmcnt(14)
	v_mul_f32_e32 v7, 0x42800000, v110
	v_mov_b32_e32 v3, v131
	v_cvt_pk_fp8_f32 v3, v4, v7
	v_mul_f32_e32 v5, 0x42800000, v122
	v_mul_f32_e32 v6, 0x42800000, v126
	v_cvt_pk_fp8_f32 v2, v5, v6 op_sel:[0,0,1]
	s_waitcnt vmcnt(13)
	v_mul_f32_e32 v4, 0x42800000, v98
	s_waitcnt vmcnt(12)
	v_mul_f32_e32 v5, 0x42800000, v102
	v_cvt_pk_fp8_f32 v3, v4, v5 op_sel:[0,0,1]
	s_waitcnt vmcnt(11)
	v_mul_f32_e32 v5, 0x42800000, v50
	s_waitcnt vmcnt(10)
	v_mul_f32_e32 v6, 0x42800000, v54
	v_mov_b32_e32 v4, v131
	v_cvt_pk_fp8_f32 v4, v5, v6
	s_waitcnt vmcnt(7)
	v_mul_f32_e32 v6, 0x42800000, v34
	s_waitcnt vmcnt(6)
	v_mul_f32_e32 v9, 0x42800000, v38
	v_mov_b32_e32 v5, v131
	v_cvt_pk_fp8_f32 v5, v6, v9
	v_mul_f32_e32 v7, 0x42800000, v66
	v_mul_f32_e32 v8, 0x42800000, v70
	v_cvt_pk_fp8_f32 v4, v7, v8 op_sel:[0,0,1]
	s_waitcnt vmcnt(5)
	v_mul_f32_e32 v6, 0x42800000, v74
	s_waitcnt vmcnt(4)
	v_mul_f32_e32 v7, 0x42800000, v78
	v_or_b32_e32 v10, s22, v134
	v_cvt_pk_fp8_f32 v5, v6, v7 op_sel:[0,0,1]
	v_ashrrev_i32_e32 v11, 31, v10
	v_lshlrev_b64 v[6:7], 10, v[10:11]
	v_lshl_add_u64 v[6:7], v[132:133], 0, v[6:7]
	global_store_dwordx4 v[6:7], v[2:5], off nt
	v_mul_f32_e32 v7, 0x42800000, v111
	v_mul_f32_e32 v6, 0x42800000, v127
	v_mul_f32_e32 v3, 0x42800000, v115
	v_mul_f32_e32 v4, 0x42800000, v119
	v_mov_b32_e32 v2, v131
	v_cvt_pk_fp8_f32 v2, v3, v4
	v_mul_f32_e32 v4, 0x42800000, v107
	v_mov_b32_e32 v3, v131
	v_cvt_pk_fp8_f32 v3, v4, v7
	v_mul_f32_e32 v5, 0x42800000, v123
	v_cvt_pk_fp8_f32 v2, v5, v6 op_sel:[0,0,1]
	v_mul_f32_e32 v4, 0x42800000, v99
	v_mul_f32_e32 v5, 0x42800000, v103
	v_cvt_pk_fp8_f32 v3, v4, v5 op_sel:[0,0,1]
	v_mul_f32_e32 v5, 0x42800000, v51
	v_mul_f32_e32 v6, 0x42800000, v55
	v_mov_b32_e32 v4, v131
	v_cvt_pk_fp8_f32 v4, v5, v6
	v_mul_f32_e32 v6, 0x42800000, v35
	v_mul_f32_e32 v9, 0x42800000, v39
	v_mov_b32_e32 v5, v131
	v_cvt_pk_fp8_f32 v5, v6, v9
	v_mul_f32_e32 v7, 0x42800000, v67
	v_mul_f32_e32 v8, 0x42800000, v71
	v_cvt_pk_fp8_f32 v4, v7, v8 op_sel:[0,0,1]
	v_mul_f32_e32 v6, 0x42800000, v75
	v_mul_f32_e32 v7, 0x42800000, v79
	v_cvt_pk_fp8_f32 v5, v6, v7 op_sel:[0,0,1]
	v_or_b32_e32 v6, 1, v10
	v_ashrrev_i32_e32 v7, 31, v6
	v_lshlrev_b64 v[6:7], 10, v[6:7]
	v_lshl_add_u64 v[6:7], v[132:133], 0, v[6:7]
	global_store_dwordx4 v[6:7], v[2:5], off nt
	v_mov_b32_e32 v6, v131
	v_mov_b32_e32 v7, v131
	v_mul_f32_e32 v2, 0x42800000, v116
	v_mul_f32_e32 v3, 0x42800000, v120
	v_cvt_pk_fp8_f32 v6, v2, v3
	v_mul_f32_e32 v2, 0x42800000, v108
	v_mul_f32_e32 v3, 0x42800000, v112
	v_cvt_pk_fp8_f32 v7, v2, v3
	v_mul_f32_e32 v2, 0x42800000, v100
	v_mul_f32_e32 v3, 0x42800000, v104
	v_mov_b32_e32 v8, v131
	v_cvt_pk_fp8_f32 v7, v2, v3 op_sel:[0,0,1]
	v_mul_f32_e32 v2, 0x42800000, v52
	v_mul_f32_e32 v3, 0x42800000, v56
	v_cvt_pk_fp8_f32 v8, v2, v3
	v_mul_f32_e32 v2, 0x42800000, v36
	v_mul_f32_e32 v3, 0x42800000, v40
	v_mov_b32_e32 v9, v131
	v_cvt_pk_fp8_f32 v9, v2, v3
	v_mul_f32_e32 v2, 0x42800000, v76
	v_mul_f32_e32 v3, 0x42800000, v80
	v_mul_f32_e32 v4, 0x42800000, v124
	v_cvt_pk_fp8_f32 v9, v2, v3 op_sel:[0,0,1]
	v_or_b32_e32 v2, 2, v10
	v_mul_f32_e32 v5, 0x42800000, v128
	v_ashrrev_i32_e32 v3, 31, v2
	v_cvt_pk_fp8_f32 v6, v4, v5 op_sel:[0,0,1]
	v_mul_f32_e32 v4, 0x42800000, v68
	v_mul_f32_e32 v5, 0x42800000, v72
	v_lshlrev_b64 v[2:3], 10, v[2:3]
	v_cvt_pk_fp8_f32 v8, v4, v5 op_sel:[0,0,1]
	v_lshl_add_u64 v[12:13], v[132:133], 0, v[2:3]
	v_mul_f32_e32 v3, 0x42800000, v117
	v_mul_f32_e32 v4, 0x42800000, v121
	v_mov_b32_e32 v2, v131
	v_cvt_pk_fp8_f32 v2, v3, v4
	v_mul_f32_e32 v4, 0x42800000, v109
	v_mul_f32_e32 v14, 0x42800000, v113
	v_mov_b32_e32 v3, v131
	v_cvt_pk_fp8_f32 v3, v4, v14
	v_mul_f32_e32 v5, 0x42800000, v125
	v_mul_f32_e32 v11, 0x42800000, v129
	v_cvt_pk_fp8_f32 v2, v5, v11 op_sel:[0,0,1]
	v_mul_f32_e32 v4, 0x42800000, v101
	v_mul_f32_e32 v5, 0x42800000, v105
	v_cvt_pk_fp8_f32 v3, v4, v5 op_sel:[0,0,1]
	v_mul_f32_e32 v5, 0x42800000, v53
	v_mul_f32_e32 v11, 0x42800000, v57
	v_mov_b32_e32 v4, v131
	v_cvt_pk_fp8_f32 v4, v5, v11
	v_mul_f32_e32 v11, 0x42800000, v37
	v_mul_f32_e32 v16, 0x42800000, v41
	v_mov_b32_e32 v5, v131
	v_cvt_pk_fp8_f32 v5, v11, v16
	v_mul_f32_e32 v14, 0x42800000, v69
	v_mul_f32_e32 v15, 0x42800000, v73
	v_cvt_pk_fp8_f32 v4, v14, v15 op_sel:[0,0,1]
	v_mul_f32_e32 v11, 0x42800000, v77
	v_mul_f32_e32 v14, 0x42800000, v81
	v_cvt_pk_fp8_f32 v5, v11, v14 op_sel:[0,0,1]
	global_store_dwordx4 v[12:13], v[6:9], off nt
	s_mov_b64 s[4:5], 0
	s_nop 0
	v_or_b32_e32 v6, 3, v10
